# out-projection GEMM K-loops (GLA and SWA): the leading wave half waits for its LDS-DMA pieces after its MFMA block instead of before it (one more barrier interval of latency cover)
# baseline (speedup 1.0000x reference)
.LBB0_689:
	s_cmp_lt_i32 s46, 7
	s_cselect_b64 s[2:3], -1, 0
	s_and_b64 s[12:13], s[2:3], s[6:7]
	s_andn2_b64 vcc, exec, s[12:13]
	s_cbranch_vccnz .LBB0_738
	v_readfirstlane_b32 s98, v0
	s_nop 0
	s_lshr_b32 s98, s98, 8
	s_cmp_eq_u32 s98, 0
	s_cselect_b64 s[98:99], -1, 0
	s_mov_b64 s[2:3], s[0:1]
	s_cmpk_lt_i32 s96, 0x400
	s_load_dwordx2 s[8:9], s[2:3], 0xc8
	s_cselect_b64 s[6:7], -1, 0
	s_cmpk_gt_i32 s96, 0x3ff
	v_readfirstlane_b32 s2, v0
	s_waitcnt lgkmcnt(0)
	s_cbranch_scc1 .LBB0_696
	s_ashr_i32 s3, s96, 31
	s_lshr_b32 s3, s3, 29
	s_add_i32 s3, s96, s3
	s_and_b32 s4, s3, -8
	s_sub_i32 s4, s96, s4
	s_cmp_gt_i32 s4, -1
	s_cbranch_scc0 .LBB0_693
	s_lshl_b32 s5, s4, 7
	s_cbranch_execz .LBB0_694
	s_branch .LBB0_695

.LBB0_712:
	ds_read_b128 v[140:143], v205
	ds_read_b128 v[144:147], v205 offset:1024
	ds_read_b128 v[148:151], v205 offset:2048
	ds_read_b128 v[152:155], v205 offset:3072
	ds_read_b128 v[182:185], v207
	ds_read_b128 v[186:189], v207 offset:1024
	ds_read_b128 v[196:199], v207 offset:2048
	ds_read_b128 v[212:215], v207 offset:3072
	s_mov_b64 s[72:73], s[56:57]
	s_add_u32 s2, s69, s72
	s_addc_u32 s74, s70, s73
	s_add_u32 s56, s72, 0x100
	s_addc_u32 s57, s73, 0
	s_cmpk_eq_i32 s72, 0xf00
	s_cselect_b64 s[58:59], -1, 0
	s_and_b64 s[60:61], s[58:59], exec
	s_cselect_b32 s61, s35, s74
	s_cselect_b32 s60, s68, s2
	s_cselect_b32 s2, 0, s56
	v_lshl_add_u64 v[4:5], v[136:137], 0, s[72:73]
	s_add_i32 m0, s42, 0xc000
	ds_read_b128 v[216:219], v210
	ds_read_b128 v[220:223], v210 offset:1024
	ds_read_b128 v[224:227], v210 offset:2048
	ds_read_b128 v[228:231], v210 offset:3072
	ds_read_b128 v[232:235], v210 offset:4096
	ds_read_b128 v[236:239], v210 offset:5120
	ds_read_b128 v[244:247], v210 offset:6144
	ds_read_b128 v[248:251], v210 offset:7168
	global_load_lds_dwordx4 v[4:5], off
	v_lshl_add_u64 v[4:5], v[134:135], 0, s[72:73]
	s_add_i32 m0, s42, 0xe000
	s_nop 0
	global_load_lds_dwordx4 v[4:5], off
	s_mov_b64 vcc, s[98:99]
	s_cbranch_vccnz .Lg0skip_1
	s_waitcnt vmcnt(8)
.Lg0skip_1:
	s_waitcnt lgkmcnt(0)
	s_barrier
	s_setprio 1
	s_waitcnt lgkmcnt(0)
	v_mfma_f32_16x16x32_bf16 v[130:133], v[140:143], v[216:219], v[130:133]
	v_mfma_f32_16x16x32_bf16 v[126:129], v[148:151], v[216:219], v[126:129]
	v_mfma_f32_16x16x32_bf16 v[114:117], v[140:143], v[224:227], v[114:117]
	v_mfma_f32_16x16x32_bf16 v[110:113], v[148:151], v[224:227], v[110:113]
	v_mfma_f32_16x16x32_bf16 v[98:101], v[140:143], v[232:235], v[98:101]
	v_mfma_f32_16x16x32_bf16 v[94:97], v[148:151], v[232:235], v[94:97]
	v_mfma_f32_16x16x32_bf16 v[82:85], v[140:143], v[244:247], v[82:85]
	v_mfma_f32_16x16x32_bf16 v[78:81], v[148:151], v[244:247], v[78:81]
	v_mfma_f32_16x16x32_bf16 v[130:133], v[144:147], v[220:223], v[130:133]
	v_mfma_f32_16x16x32_bf16 v[126:129], v[152:155], v[220:223], v[126:129]
	v_mfma_f32_16x16x32_bf16 v[114:117], v[144:147], v[228:231], v[114:117]
	v_mfma_f32_16x16x32_bf16 v[110:113], v[152:155], v[228:231], v[110:113]
	v_mfma_f32_16x16x32_bf16 v[98:101], v[144:147], v[236:239], v[98:101]
	v_mfma_f32_16x16x32_bf16 v[94:97], v[152:155], v[236:239], v[94:97]
	v_mfma_f32_16x16x32_bf16 v[82:85], v[144:147], v[248:251], v[82:85]
	v_mfma_f32_16x16x32_bf16 v[78:81], v[152:155], v[248:251], v[78:81]
	s_setprio 0
	s_setprio 1
	v_mfma_f32_16x16x32_bf16 v[122:125], v[182:185], v[216:219], v[122:125]
	v_mfma_f32_16x16x32_bf16 v[118:121], v[196:199], v[216:219], v[118:121]
	v_mfma_f32_16x16x32_bf16 v[106:109], v[182:185], v[224:227], v[106:109]
	v_mfma_f32_16x16x32_bf16 v[102:105], v[196:199], v[224:227], v[102:105]
	v_mfma_f32_16x16x32_bf16 v[90:93], v[182:185], v[232:235], v[90:93]
	v_mfma_f32_16x16x32_bf16 v[86:89], v[196:199], v[232:235], v[86:89]
	v_mfma_f32_16x16x32_bf16 v[74:77], v[182:185], v[244:247], v[74:77]
	v_mfma_f32_16x16x32_bf16 v[70:73], v[196:199], v[244:247], v[70:73]
	v_mfma_f32_16x16x32_bf16 v[122:125], v[186:189], v[220:223], v[122:125]
	v_mfma_f32_16x16x32_bf16 v[118:121], v[212:215], v[220:223], v[118:121]
	v_mfma_f32_16x16x32_bf16 v[106:109], v[186:189], v[228:231], v[106:109]
	v_mfma_f32_16x16x32_bf16 v[102:105], v[212:215], v[228:231], v[102:105]
	v_mfma_f32_16x16x32_bf16 v[90:93], v[186:189], v[236:239], v[90:93]
	v_mfma_f32_16x16x32_bf16 v[86:89], v[212:215], v[236:239], v[86:89]
	v_mfma_f32_16x16x32_bf16 v[74:77], v[186:189], v[248:251], v[74:77]
	v_mfma_f32_16x16x32_bf16 v[70:73], v[212:215], v[248:251], v[70:73]
	s_setprio 0
	s_mov_b64 vcc, s[98:99]
	s_cbranch_vccz .Lg0m_1
	s_waitcnt vmcnt(8)
.Lg0m_1:
	s_barrier
	s_add_i32 s72, s63, s15
	v_lshl_add_u64 v[156:157], s[60:61], 0, v[160:161]
	s_mov_b32 m0, s72
	ds_read_b128 v[216:219], v210 offset:16384
	ds_read_b128 v[220:223], v210 offset:17408
	ds_read_b128 v[224:227], v210 offset:18432
	ds_read_b128 v[228:231], v210 offset:19456
	ds_read_b128 v[232:235], v210 offset:20480
	ds_read_b128 v[236:239], v210 offset:21504
	ds_read_b128 v[244:247], v210 offset:22528
	ds_read_b128 v[248:251], v210 offset:23552
	global_load_lds_dwordx4 v[156:157], off
	s_add_i32 m0, s72, 0x2000
	s_add_u32 s72, s60, 0x80000
	v_lshl_add_u64 v[178:179], s[60:61], 0, v[164:165]
	s_addc_u32 s73, s61, 0
	s_add_i32 s74, s64, s15
	global_load_lds_dwordx4 v[178:179], off
	v_lshl_add_u64 v[4:5], s[72:73], 0, v[160:161]
	s_mov_b32 m0, s74
	s_nop 0
	global_load_lds_dwordx4 v[4:5], off
	v_lshl_add_u64 v[4:5], s[72:73], 0, v[164:165]
	s_add_i32 m0, s74, 0x2000
	s_and_b64 s[72:73], s[10:11], s[58:59]
	s_and_b64 s[72:73], s[72:73], exec
	s_cselect_b32 s72, s38, s54
	s_cselect_b32 s73, s39, s55
	s_add_u32 s72, s72, s2
	s_addc_u32 s73, s73, 0
	global_load_lds_dwordx4 v[4:5], off
	v_lshl_add_u64 v[192:193], s[72:73], 0, v[158:159]
	s_mov_b32 m0, s42
	v_lshl_add_u64 v[202:203], s[72:73], 0, v[162:163]
	global_load_lds_dwordx4 v[192:193], off
	s_mov_b32 m0, s43
	s_nop 0
	global_load_lds_dwordx4 v[202:203], off
	s_mov_b64 vcc, s[98:99]
	s_cbranch_vccnz .Lg0skip_2
	s_waitcnt vmcnt(8)
.Lg0skip_2:
	s_waitcnt lgkmcnt(0)
	s_barrier
	s_setprio 1
	s_waitcnt lgkmcnt(0)
	v_mfma_f32_16x16x32_bf16 v[66:69], v[140:143], v[216:219], v[66:69]
	v_mfma_f32_16x16x32_bf16 v[62:65], v[148:151], v[216:219], v[62:65]
	v_mfma_f32_16x16x32_bf16 v[50:53], v[140:143], v[224:227], v[50:53]
	v_mfma_f32_16x16x32_bf16 v[46:49], v[148:151], v[224:227], v[46:49]
	v_mfma_f32_16x16x32_bf16 v[34:37], v[140:143], v[232:235], v[34:37]
	v_mfma_f32_16x16x32_bf16 v[30:33], v[148:151], v[232:235], v[30:33]
	v_mfma_f32_16x16x32_bf16 v[18:21], v[140:143], v[244:247], v[18:21]
	v_mfma_f32_16x16x32_bf16 v[14:17], v[148:151], v[244:247], v[14:17]
	v_mfma_f32_16x16x32_bf16 v[66:69], v[144:147], v[220:223], v[66:69]
	v_mfma_f32_16x16x32_bf16 v[62:65], v[152:155], v[220:223], v[62:65]
	v_mfma_f32_16x16x32_bf16 v[50:53], v[144:147], v[228:231], v[50:53]
	v_mfma_f32_16x16x32_bf16 v[46:49], v[152:155], v[228:231], v[46:49]
	v_mfma_f32_16x16x32_bf16 v[34:37], v[144:147], v[236:239], v[34:37]
	v_mfma_f32_16x16x32_bf16 v[30:33], v[152:155], v[236:239], v[30:33]
	v_mfma_f32_16x16x32_bf16 v[18:21], v[144:147], v[248:251], v[18:21]
	v_mfma_f32_16x16x32_bf16 v[14:17], v[152:155], v[248:251], v[14:17]
	s_setprio 0
	s_setprio 1
	v_mfma_f32_16x16x32_bf16 v[58:61], v[182:185], v[216:219], v[58:61]
	v_mfma_f32_16x16x32_bf16 v[54:57], v[196:199], v[216:219], v[54:57]
	v_mfma_f32_16x16x32_bf16 v[42:45], v[182:185], v[224:227], v[42:45]
	v_mfma_f32_16x16x32_bf16 v[38:41], v[196:199], v[224:227], v[38:41]
	v_mfma_f32_16x16x32_bf16 v[26:29], v[182:185], v[232:235], v[26:29]
	v_mfma_f32_16x16x32_bf16 v[22:25], v[196:199], v[232:235], v[22:25]
	v_mfma_f32_16x16x32_bf16 v[10:13], v[182:185], v[244:247], v[10:13]
	v_mfma_f32_16x16x32_bf16 v[4:7], v[196:199], v[244:247], v[6:9]
	v_mfma_f32_16x16x32_bf16 v[58:61], v[186:189], v[220:223], v[58:61]
	v_mfma_f32_16x16x32_bf16 v[54:57], v[212:215], v[220:223], v[54:57]
	v_mfma_f32_16x16x32_bf16 v[42:45], v[186:189], v[228:231], v[42:45]
	v_mfma_f32_16x16x32_bf16 v[38:41], v[212:215], v[228:231], v[38:41]
	v_mfma_f32_16x16x32_bf16 v[26:29], v[186:189], v[236:239], v[26:29]
	v_mfma_f32_16x16x32_bf16 v[22:25], v[212:215], v[236:239], v[22:25]
	v_mfma_f32_16x16x32_bf16 v[10:13], v[186:189], v[248:251], v[10:13]
	v_mfma_f32_16x16x32_bf16 v[4:7], v[212:215], v[248:251], v[4:7]
	s_setprio 0
	s_mov_b64 vcc, s[98:99]
	s_cbranch_vccz .Lg0m_2
	s_waitcnt vmcnt(8)
.Lg0m_2:
	s_barrier
	s_add_i32 s2, 0, 0x18000
	v_add_u32_e32 v3, s2, v177
	s_add_i32 s74, 0, 0x1c000
	ds_read_b128 v[140:143], v3
	ds_read_b128 v[144:147], v3 offset:1024
	ds_read_b128 v[148:151], v3 offset:2048
	ds_read_b128 v[152:155], v3 offset:3072
	v_add_u32_e32 v3, s74, v177
	ds_read_b128 v[182:185], v3
	ds_read_b128 v[186:189], v3 offset:1024
	ds_read_b128 v[196:199], v3 offset:2048
	ds_read_b128 v[212:215], v3 offset:3072
	s_add_u32 s72, s72, 0x80000
	s_addc_u32 s73, s73, 0
	s_mov_b32 m0, s48
	v_lshl_add_u64 v[8:9], s[72:73], 0, v[158:159]
	ds_read_b128 v[216:219], v210 offset:32768
	ds_read_b128 v[220:223], v210 offset:33792
	ds_read_b128 v[224:227], v210 offset:34816
	ds_read_b128 v[228:231], v210 offset:35840
	ds_read_b128 v[232:235], v210 offset:36864
	ds_read_b128 v[236:239], v210 offset:37888
	ds_read_b128 v[244:247], v210 offset:38912
	ds_read_b128 v[248:251], v210 offset:39936
	global_load_lds_dwordx4 v[8:9], off
	v_lshl_add_u64 v[8:9], s[72:73], 0, v[162:163]
	s_mov_b32 m0, s49
	s_nop 0
	global_load_lds_dwordx4 v[8:9], off
	s_mov_b64 vcc, s[98:99]
	s_cbranch_vccnz .Lg0skip_3
	s_waitcnt vmcnt(8)

.Lg0m_3:
	s_barrier
	s_add_i32 s2, s2, s15
	v_lshl_add_u64 v[8:9], v[156:157], 0, s[28:29]
	s_mov_b32 m0, s2
	ds_read_b128 v[216:219], v210 offset:49152
	ds_read_b128 v[220:223], v210 offset:50176
	ds_read_b128 v[224:227], v210 offset:51200
	ds_read_b128 v[228:231], v210 offset:52224
	ds_read_b128 v[232:235], v210 offset:53248
	ds_read_b128 v[236:239], v210 offset:54272
	ds_read_b128 v[244:247], v210 offset:55296
	ds_read_b128 v[248:251], v210 offset:56320
	global_load_lds_dwordx4 v[8:9], off
	s_add_i32 m0, s2, 0x2000
	s_add_u32 s60, s60, 0x80080
	v_lshl_add_u64 v[8:9], v[178:179], 0, s[28:29]
	s_addc_u32 s61, s61, 0
	s_add_i32 s2, s74, s15
	global_load_lds_dwordx4 v[8:9], off
	v_lshl_add_u64 v[8:9], s[60:61], 0, v[160:161]
	s_mov_b32 m0, s2
	s_nop 0
	global_load_lds_dwordx4 v[8:9], off
	v_lshl_add_u64 v[8:9], s[60:61], 0, v[164:165]
	s_add_i32 m0, s2, 0x2000
	s_nop 0
	global_load_lds_dwordx4 v[8:9], off
	v_lshl_add_u64 v[8:9], v[192:193], 0, s[28:29]
	s_mov_b32 m0, s51
	s_nop 0
	global_load_lds_dwordx4 v[8:9], off
	v_lshl_add_u64 v[8:9], v[202:203], 0, s[28:29]
	s_mov_b32 m0, s52
	s_nop 0
	global_load_lds_dwordx4 v[8:9], off
	s_mov_b64 vcc, s[98:99]
	s_cbranch_vccnz .Lg0skip_4
	s_waitcnt vmcnt(8)
.Lg0skip_4:
	s_waitcnt lgkmcnt(0)
	s_barrier
	s_setprio 1
	s_waitcnt lgkmcnt(0)
	v_mfma_f32_16x16x32_bf16 v[66:69], v[140:143], v[216:219], v[66:69]
	v_mfma_f32_16x16x32_bf16 v[62:65], v[148:151], v[216:219], v[62:65]
	v_mfma_f32_16x16x32_bf16 v[50:53], v[140:143], v[224:227], v[50:53]
	v_mfma_f32_16x16x32_bf16 v[46:49], v[148:151], v[224:227], v[46:49]
	v_mfma_f32_16x16x32_bf16 v[34:37], v[140:143], v[232:235], v[34:37]
	v_mfma_f32_16x16x32_bf16 v[30:33], v[148:151], v[232:235], v[30:33]
	v_mfma_f32_16x16x32_bf16 v[18:21], v[140:143], v[244:247], v[18:21]
	v_mfma_f32_16x16x32_bf16 v[14:17], v[148:151], v[244:247], v[14:17]
	v_mfma_f32_16x16x32_bf16 v[66:69], v[144:147], v[220:223], v[66:69]
	v_mfma_f32_16x16x32_bf16 v[62:65], v[152:155], v[220:223], v[62:65]
	v_mfma_f32_16x16x32_bf16 v[50:53], v[144:147], v[228:231], v[50:53]
	v_mfma_f32_16x16x32_bf16 v[46:49], v[152:155], v[228:231], v[46:49]
	v_mfma_f32_16x16x32_bf16 v[34:37], v[144:147], v[236:239], v[34:37]
	v_mfma_f32_16x16x32_bf16 v[30:33], v[152:155], v[236:239], v[30:33]
	v_mfma_f32_16x16x32_bf16 v[18:21], v[144:147], v[248:251], v[18:21]
	v_mfma_f32_16x16x32_bf16 v[14:17], v[152:155], v[248:251], v[14:17]
	s_setprio 0
	s_setprio 1
	v_mfma_f32_16x16x32_bf16 v[58:61], v[182:185], v[216:219], v[58:61]
	v_mfma_f32_16x16x32_bf16 v[54:57], v[196:199], v[216:219], v[54:57]
	v_mfma_f32_16x16x32_bf16 v[42:45], v[182:185], v[224:227], v[42:45]
	v_mfma_f32_16x16x32_bf16 v[38:41], v[196:199], v[224:227], v[38:41]
	v_mfma_f32_16x16x32_bf16 v[26:29], v[182:185], v[232:235], v[26:29]
	v_mfma_f32_16x16x32_bf16 v[22:25], v[196:199], v[232:235], v[22:25]
	v_mfma_f32_16x16x32_bf16 v[8:11], v[182:185], v[244:247], v[10:13]
	v_mfma_f32_16x16x32_bf16 v[4:7], v[196:199], v[244:247], v[4:7]
	v_mfma_f32_16x16x32_bf16 v[58:61], v[186:189], v[220:223], v[58:61]
	v_mfma_f32_16x16x32_bf16 v[54:57], v[212:215], v[220:223], v[54:57]
	v_mfma_f32_16x16x32_bf16 v[42:45], v[186:189], v[228:231], v[42:45]
	v_mfma_f32_16x16x32_bf16 v[38:41], v[212:215], v[228:231], v[38:41]
	v_mfma_f32_16x16x32_bf16 v[26:29], v[186:189], v[236:239], v[26:29]
	v_mfma_f32_16x16x32_bf16 v[22:25], v[212:215], v[236:239], v[22:25]
	v_mfma_f32_16x16x32_bf16 v[10:13], v[186:189], v[248:251], v[8:11]
	v_mfma_f32_16x16x32_bf16 v[6:9], v[212:215], v[248:251], v[4:7]
	s_setprio 0
	s_mov_b64 vcc, s[98:99]
	s_cbranch_vccz .Lg0m_4
	s_waitcnt vmcnt(8)
.Lg0m_4:
	s_barrier
	s_add_i32 s2, s71, 4
	s_and_b32 s2, s2, 6
	s_cmp_lg_u32 s2, 0
	s_cselect_b64 s[60:61], -1, 0
	s_or_b64 s[58:59], s[58:59], s[60:61]
	s_and_b64 vcc, exec, s[58:59]
	s_cbranch_vccnz .LBB0_711
	ds_read2st64_b32 v[4:5], v138 offset1:1
	ds_read2st64_b32 v[140:141], v138 offset0:2 offset1:3
	ds_read2st64_b32 v[142:143], v138 offset0:8 offset1:9
	ds_read2st64_b32 v[144:145], v138 offset0:10 offset1:11
	s_waitcnt lgkmcnt(0)
	v_pk_mul_f32 v[132:133], v[132:133], v[4:5] op_sel_hi:[1,0]
	v_pk_mul_f32 v[130:131], v[130:131], v[4:5] op_sel_hi:[1,0]
	v_pk_mul_f32 v[128:129], v[128:129], v[4:5] op_sel_hi:[1,0]
	v_pk_mul_f32 v[126:127], v[126:127], v[4:5] op_sel_hi:[1,0]
	v_pk_mul_f32 v[124:125], v[124:125], v[4:5] op_sel_hi:[1,0]
	v_pk_mul_f32 v[122:123], v[122:123], v[4:5] op_sel_hi:[1,0]
	v_pk_mul_f32 v[120:121], v[120:121], v[4:5] op_sel_hi:[1,0]
	v_pk_mul_f32 v[118:119], v[118:119], v[4:5] op_sel_hi:[1,0]
	v_mov_b32_e32 v4, v5
	v_pk_mul_f32 v[116:117], v[116:117], v[4:5] op_sel_hi:[1,0]
	v_pk_mul_f32 v[114:115], v[114:115], v[4:5] op_sel_hi:[1,0]
	v_pk_mul_f32 v[112:113], v[112:113], v[4:5] op_sel_hi:[1,0]
	v_pk_mul_f32 v[110:111], v[110:111], v[4:5] op_sel_hi:[1,0]
	v_pk_mul_f32 v[108:109], v[108:109], v[4:5] op_sel_hi:[1,0]
	v_pk_mul_f32 v[106:107], v[106:107], v[4:5] op_sel_hi:[1,0]
	v_pk_mul_f32 v[104:105], v[104:105], v[4:5] op_sel_hi:[1,0]
	v_pk_mul_f32 v[102:103], v[102:103], v[4:5] op_sel_hi:[1,0]
	v_mov_b32_e32 v4, v141
	v_pk_mul_f32 v[84:85], v[84:85], v[4:5] op_sel_hi:[1,0]
	v_pk_mul_f32 v[82:83], v[82:83], v[4:5] op_sel_hi:[1,0]
	v_pk_mul_f32 v[80:81], v[80:81], v[4:5] op_sel_hi:[1,0]
	v_pk_mul_f32 v[78:79], v[78:79], v[4:5] op_sel_hi:[1,0]
	v_pk_mul_f32 v[76:77], v[76:77], v[4:5] op_sel_hi:[1,0]
	v_pk_mul_f32 v[74:75], v[74:75], v[4:5] op_sel_hi:[1,0]
	v_pk_mul_f32 v[72:73], v[72:73], v[4:5] op_sel_hi:[1,0]
	v_pk_mul_f32 v[70:71], v[70:71], v[4:5] op_sel_hi:[1,0]
	v_mov_b32_e32 v4, v143
	v_pk_mul_f32 v[52:53], v[52:53], v[4:5] op_sel_hi:[1,0]
	v_pk_mul_f32 v[50:51], v[50:51], v[4:5] op_sel_hi:[1,0]
	v_pk_mul_f32 v[48:49], v[48:49], v[4:5] op_sel_hi:[1,0]
	v_pk_mul_f32 v[46:47], v[46:47], v[4:5] op_sel_hi:[1,0]
	v_pk_mul_f32 v[44:45], v[44:45], v[4:5] op_sel_hi:[1,0]
	v_pk_mul_f32 v[42:43], v[42:43], v[4:5] op_sel_hi:[1,0]
	v_pk_mul_f32 v[40:41], v[40:41], v[4:5] op_sel_hi:[1,0]
	v_pk_mul_f32 v[38:39], v[38:39], v[4:5] op_sel_hi:[1,0]
	v_mov_b32_e32 v4, v145
	v_pk_mul_f32 v[100:101], v[100:101], v[140:141] op_sel_hi:[1,0]
	v_pk_mul_f32 v[98:99], v[98:99], v[140:141] op_sel_hi:[1,0]
	v_pk_mul_f32 v[96:97], v[96:97], v[140:141] op_sel_hi:[1,0]
	v_pk_mul_f32 v[94:95], v[94:95], v[140:141] op_sel_hi:[1,0]
	v_pk_mul_f32 v[92:93], v[92:93], v[140:141] op_sel_hi:[1,0]
	v_pk_mul_f32 v[90:91], v[90:91], v[140:141] op_sel_hi:[1,0]
	v_pk_mul_f32 v[88:89], v[88:89], v[140:141] op_sel_hi:[1,0]
	v_pk_mul_f32 v[86:87], v[86:87], v[140:141] op_sel_hi:[1,0]
	v_pk_mul_f32 v[68:69], v[68:69], v[142:143] op_sel_hi:[1,0]
	v_pk_mul_f32 v[66:67], v[66:67], v[142:143] op_sel_hi:[1,0]
	v_pk_mul_f32 v[64:65], v[64:65], v[142:143] op_sel_hi:[1,0]
	v_pk_mul_f32 v[62:63], v[62:63], v[142:143] op_sel_hi:[1,0]
	v_pk_mul_f32 v[60:61], v[60:61], v[142:143] op_sel_hi:[1,0]
	v_pk_mul_f32 v[58:59], v[58:59], v[142:143] op_sel_hi:[1,0]
	v_pk_mul_f32 v[56:57], v[56:57], v[142:143] op_sel_hi:[1,0]
	v_pk_mul_f32 v[54:55], v[54:55], v[142:143] op_sel_hi:[1,0]
	v_pk_mul_f32 v[36:37], v[36:37], v[144:145] op_sel_hi:[1,0]
	v_pk_mul_f32 v[34:35], v[34:35], v[144:145] op_sel_hi:[1,0]
	v_pk_mul_f32 v[32:33], v[32:33], v[144:145] op_sel_hi:[1,0]
	v_pk_mul_f32 v[30:31], v[30:31], v[144:145] op_sel_hi:[1,0]
	v_pk_mul_f32 v[28:29], v[28:29], v[144:145] op_sel_hi:[1,0]
	v_pk_mul_f32 v[26:27], v[26:27], v[144:145] op_sel_hi:[1,0]
	v_pk_mul_f32 v[24:25], v[24:25], v[144:145] op_sel_hi:[1,0]
	v_pk_mul_f32 v[22:23], v[22:23], v[144:145] op_sel_hi:[1,0]
	v_pk_mul_f32 v[20:21], v[20:21], v[4:5] op_sel_hi:[1,0]
	v_pk_mul_f32 v[18:19], v[18:19], v[4:5] op_sel_hi:[1,0]
	v_pk_mul_f32 v[16:17], v[16:17], v[4:5] op_sel_hi:[1,0]
	v_pk_mul_f32 v[14:15], v[14:15], v[4:5] op_sel_hi:[1,0]
	v_pk_mul_f32 v[12:13], v[12:13], v[4:5] op_sel_hi:[1,0]
	v_pk_mul_f32 v[10:11], v[10:11], v[4:5] op_sel_hi:[1,0]
	v_pk_mul_f32 v[8:9], v[8:9], v[4:5] op_sel_hi:[1,0]
	v_pk_mul_f32 v[6:7], v[6:7], v[4:5] op_sel_hi:[1,0]
	s_branch .LBB0_711

.LBB0_1527:
	s_cmp_lt_i32 s46, 16
	s_cselect_b64 s[2:3], -1, 0
	s_and_b64 s[10:11], s[2:3], s[6:7]
	s_andn2_b64 vcc, exec, s[10:11]
	s_cbranch_vccnz .LBB0_1570
	v_readfirstlane_b32 s98, v0
	s_nop 0
	s_lshr_b32 s98, s98, 8
	s_cmp_eq_u32 s98, 0
	s_cselect_b64 s[98:99], -1, 0
	s_mov_b64 s[2:3], s[0:1]
	s_cmpk_lt_i32 s96, 0x400
	s_load_dwordx2 s[6:7], s[2:3], 0xc8
	s_cselect_b64 s[8:9], -1, 0
	s_cmpk_gt_i32 s96, 0x3ff
	v_readfirstlane_b32 s2, v0
	s_waitcnt lgkmcnt(0)
	s_cbranch_scc1 .LBB0_1534
	s_ashr_i32 s3, s96, 31
	s_lshr_b32 s3, s3, 29
	s_add_i32 s3, s96, s3
	s_and_b32 s4, s3, -8
	s_sub_i32 s4, s96, s4
	s_cmp_gt_i32 s4, -1
	s_cbranch_scc0 .LBB0_1531
	s_lshl_b32 s5, s4, 7
	s_cbranch_execz .LBB0_1532
	s_branch .LBB0_1533

.LBB0_1547:
	ds_read_b128 v[134:137], v189
	ds_read_b128 v[138:141], v189 offset:1024
	ds_read_b128 v[142:145], v189 offset:2048
	ds_read_b128 v[146:149], v189 offset:3072
	ds_read_b128 v[150:153], v190
	ds_read_b128 v[170:173], v190 offset:1024
	ds_read_b128 v[174:177], v190 offset:2048
	ds_read_b128 v[194:197], v190 offset:3072
	s_add_u32 s2, s66, s54
	s_addc_u32 s69, s67, s55
	s_add_u32 s56, s54, 0x100
	s_addc_u32 s57, s55, 0
	s_cmp_eq_u32 s68, 28
	s_cselect_b64 s[60:61], -1, 0
	s_and_b64 s[58:59], s[60:61], exec
	s_cselect_b32 s59, s31, s69
	s_cselect_b32 s58, s35, s2
	s_cselect_b32 s2, 0, s56
	v_lshl_add_u64 v[178:179], v[130:131], 0, s[54:55]
	s_add_i32 m0, s13, 0xc000
	ds_read_b128 v[198:201], v191
	ds_read_b128 v[202:205], v191 offset:1024
	ds_read_b128 v[206:209], v191 offset:2048
	ds_read_b128 v[210:213], v191 offset:3072
	ds_read_b128 v[214:217], v191 offset:4096
	ds_read_b128 v[218:221], v191 offset:5120
	ds_read_b128 v[222:225], v191 offset:6144
	ds_read_b128 v[226:229], v191 offset:7168
	global_load_lds_dwordx4 v[178:179], off
	v_lshl_add_u64 v[178:179], v[132:133], 0, s[54:55]
	s_add_i32 m0, s13, 0xe000
	s_nop 0
	global_load_lds_dwordx4 v[178:179], off
	s_mov_b64 vcc, s[98:99]
	s_cbranch_vccnz .Lg0skip_5
	s_waitcnt vmcnt(8)
.Lg0skip_5:
	s_waitcnt lgkmcnt(0)
	s_barrier
	s_setprio 1
	s_waitcnt lgkmcnt(0)
	v_mfma_f32_16x16x32_bf16 v[126:129], v[134:137], v[198:201], v[126:129]
	v_mfma_f32_16x16x32_bf16 v[122:125], v[142:145], v[198:201], v[122:125]
	v_mfma_f32_16x16x32_bf16 v[110:113], v[134:137], v[206:209], v[110:113]
	v_mfma_f32_16x16x32_bf16 v[106:109], v[142:145], v[206:209], v[106:109]
	v_mfma_f32_16x16x32_bf16 v[94:97], v[134:137], v[214:217], v[94:97]
	v_mfma_f32_16x16x32_bf16 v[90:93], v[142:145], v[214:217], v[90:93]
	v_mfma_f32_16x16x32_bf16 v[78:81], v[134:137], v[222:225], v[78:81]
	v_mfma_f32_16x16x32_bf16 v[74:77], v[142:145], v[222:225], v[74:77]
	v_mfma_f32_16x16x32_bf16 v[126:129], v[138:141], v[202:205], v[126:129]
	v_mfma_f32_16x16x32_bf16 v[122:125], v[146:149], v[202:205], v[122:125]
	v_mfma_f32_16x16x32_bf16 v[110:113], v[138:141], v[210:213], v[110:113]
	v_mfma_f32_16x16x32_bf16 v[106:109], v[146:149], v[210:213], v[106:109]
	v_mfma_f32_16x16x32_bf16 v[94:97], v[138:141], v[218:221], v[94:97]
	v_mfma_f32_16x16x32_bf16 v[90:93], v[146:149], v[218:221], v[90:93]
	v_mfma_f32_16x16x32_bf16 v[78:81], v[138:141], v[226:229], v[78:81]
	v_mfma_f32_16x16x32_bf16 v[74:77], v[146:149], v[226:229], v[74:77]
	s_setprio 0
	s_setprio 1
	v_mfma_f32_16x16x32_bf16 v[118:121], v[150:153], v[198:201], v[118:121]
	v_mfma_f32_16x16x32_bf16 v[114:117], v[174:177], v[198:201], v[114:117]
	v_mfma_f32_16x16x32_bf16 v[102:105], v[150:153], v[206:209], v[102:105]
	v_mfma_f32_16x16x32_bf16 v[98:101], v[174:177], v[206:209], v[98:101]
	v_mfma_f32_16x16x32_bf16 v[86:89], v[150:153], v[214:217], v[86:89]
	v_mfma_f32_16x16x32_bf16 v[82:85], v[174:177], v[214:217], v[82:85]
	v_mfma_f32_16x16x32_bf16 v[70:73], v[150:153], v[222:225], v[70:73]
	v_mfma_f32_16x16x32_bf16 v[66:69], v[174:177], v[222:225], v[66:69]
	v_mfma_f32_16x16x32_bf16 v[118:121], v[170:173], v[202:205], v[118:121]
	v_mfma_f32_16x16x32_bf16 v[114:117], v[194:197], v[202:205], v[114:117]
	v_mfma_f32_16x16x32_bf16 v[102:105], v[170:173], v[210:213], v[102:105]
	v_mfma_f32_16x16x32_bf16 v[98:101], v[194:197], v[210:213], v[98:101]
	v_mfma_f32_16x16x32_bf16 v[86:89], v[170:173], v[218:221], v[86:89]
	v_mfma_f32_16x16x32_bf16 v[82:85], v[194:197], v[218:221], v[82:85]
	v_mfma_f32_16x16x32_bf16 v[70:73], v[170:173], v[226:229], v[70:73]
	v_mfma_f32_16x16x32_bf16 v[66:69], v[194:197], v[226:229], v[66:69]
	s_setprio 0
	s_mov_b64 vcc, s[98:99]
	s_cbranch_vccz .Lg0m_5
	s_waitcnt vmcnt(8)
.Lg0m_5:
	s_barrier
	s_add_i32 s54, s63, s42
	v_lshl_add_u64 v[178:179], s[58:59], 0, v[156:157]
	s_mov_b32 m0, s54
	ds_read_b128 v[198:201], v191 offset:16384
	ds_read_b128 v[202:205], v191 offset:17408
	ds_read_b128 v[206:209], v191 offset:18432
	ds_read_b128 v[210:213], v191 offset:19456
	ds_read_b128 v[214:217], v191 offset:20480
	ds_read_b128 v[218:221], v191 offset:21504
	ds_read_b128 v[222:225], v191 offset:22528
	ds_read_b128 v[226:229], v191 offset:23552
	global_load_lds_dwordx4 v[178:179], off
	s_add_i32 m0, s54, 0x2000
	s_add_u32 s54, s58, 0x80000
	v_lshl_add_u64 v[182:183], s[58:59], 0, v[160:161]
	s_addc_u32 s55, s59, 0
	s_add_i32 s69, s64, s42
	global_load_lds_dwordx4 v[182:183], off
	v_lshl_add_u64 v[186:187], s[54:55], 0, v[156:157]
	s_mov_b32 m0, s69
	s_nop 0
	global_load_lds_dwordx4 v[186:187], off
	v_lshl_add_u64 v[186:187], s[54:55], 0, v[160:161]
	s_add_i32 m0, s69, 0x2000
	s_and_b64 s[54:55], s[8:9], s[60:61]
	s_and_b64 s[54:55], s[54:55], exec
	s_cselect_b32 s54, s36, s40
	s_cselect_b32 s55, s37, s41
	s_add_u32 s54, s54, s2
	s_addc_u32 s55, s55, 0
	global_load_lds_dwordx4 v[186:187], off
	v_lshl_add_u64 v[186:187], s[54:55], 0, v[154:155]
	s_mov_b32 m0, s13
	v_lshl_add_u64 v[230:231], s[54:55], 0, v[158:159]
	global_load_lds_dwordx4 v[186:187], off
	s_mov_b32 m0, s43
	s_nop 0
	global_load_lds_dwordx4 v[230:231], off
	s_mov_b64 vcc, s[98:99]
	s_cbranch_vccnz .Lg0skip_6
	s_waitcnt vmcnt(8)
.Lg0skip_6:
	s_waitcnt lgkmcnt(0)
	s_barrier
	s_setprio 1
	s_waitcnt lgkmcnt(0)
	v_mfma_f32_16x16x32_bf16 v[62:65], v[134:137], v[198:201], v[62:65]
	v_mfma_f32_16x16x32_bf16 v[58:61], v[142:145], v[198:201], v[58:61]
	v_mfma_f32_16x16x32_bf16 v[46:49], v[134:137], v[206:209], v[46:49]
	v_mfma_f32_16x16x32_bf16 v[42:45], v[142:145], v[206:209], v[42:45]
	v_mfma_f32_16x16x32_bf16 v[30:33], v[134:137], v[214:217], v[30:33]
	v_mfma_f32_16x16x32_bf16 v[26:29], v[142:145], v[214:217], v[26:29]
	v_mfma_f32_16x16x32_bf16 v[14:17], v[134:137], v[222:225], v[14:17]
	v_mfma_f32_16x16x32_bf16 v[10:13], v[142:145], v[222:225], v[10:13]
	v_mfma_f32_16x16x32_bf16 v[62:65], v[138:141], v[202:205], v[62:65]
	v_mfma_f32_16x16x32_bf16 v[58:61], v[146:149], v[202:205], v[58:61]
	v_mfma_f32_16x16x32_bf16 v[46:49], v[138:141], v[210:213], v[46:49]
	v_mfma_f32_16x16x32_bf16 v[42:45], v[146:149], v[210:213], v[42:45]
	v_mfma_f32_16x16x32_bf16 v[30:33], v[138:141], v[218:221], v[30:33]
	v_mfma_f32_16x16x32_bf16 v[26:29], v[146:149], v[218:221], v[26:29]
	v_mfma_f32_16x16x32_bf16 v[14:17], v[138:141], v[226:229], v[14:17]
	v_mfma_f32_16x16x32_bf16 v[10:13], v[146:149], v[226:229], v[10:13]
	s_setprio 0
	s_setprio 1
	v_mfma_f32_16x16x32_bf16 v[54:57], v[150:153], v[198:201], v[54:57]
	v_mfma_f32_16x16x32_bf16 v[50:53], v[174:177], v[198:201], v[50:53]
	v_mfma_f32_16x16x32_bf16 v[38:41], v[150:153], v[206:209], v[38:41]
	v_mfma_f32_16x16x32_bf16 v[34:37], v[174:177], v[206:209], v[34:37]
	v_mfma_f32_16x16x32_bf16 v[22:25], v[150:153], v[214:217], v[22:25]
	v_mfma_f32_16x16x32_bf16 v[18:21], v[174:177], v[214:217], v[18:21]
	v_mfma_f32_16x16x32_bf16 v[6:9], v[150:153], v[222:225], v[6:9]
	v_mfma_f32_16x16x32_bf16 v[2:5], v[174:177], v[222:225], v[2:5]
	v_mfma_f32_16x16x32_bf16 v[54:57], v[170:173], v[202:205], v[54:57]
	v_mfma_f32_16x16x32_bf16 v[50:53], v[194:197], v[202:205], v[50:53]
	v_mfma_f32_16x16x32_bf16 v[38:41], v[170:173], v[210:213], v[38:41]
	v_mfma_f32_16x16x32_bf16 v[34:37], v[194:197], v[210:213], v[34:37]
	v_mfma_f32_16x16x32_bf16 v[22:25], v[170:173], v[218:221], v[22:25]
	v_mfma_f32_16x16x32_bf16 v[18:21], v[194:197], v[218:221], v[18:21]
	v_mfma_f32_16x16x32_bf16 v[6:9], v[170:173], v[226:229], v[6:9]
	v_mfma_f32_16x16x32_bf16 v[2:5], v[194:197], v[226:229], v[2:5]
	s_setprio 0
	s_mov_b64 vcc, s[98:99]
	s_cbranch_vccz .Lg0m_6
	s_waitcnt vmcnt(8)
.Lg0m_6:
	s_barrier
	s_add_i32 s2, 0, 0x18000
	s_add_i32 s60, 0, 0x1c000
	v_add_u32_e32 v146, s2, v181
	v_add_u32_e32 v180, s60, v181
	ds_read_b128 v[134:137], v146
	ds_read_b128 v[138:141], v146 offset:1024
	ds_read_b128 v[142:145], v146 offset:2048
	ds_read_b128 v[146:149], v146 offset:3072
	ds_read_b128 v[150:153], v180
	ds_read_b128 v[170:173], v180 offset:1024
	ds_read_b128 v[174:177], v180 offset:2048
	ds_read_b128 v[194:197], v180 offset:3072
	s_add_u32 s54, s54, 0x80000
	s_addc_u32 s55, s55, 0
	s_mov_b32 m0, s48
	v_lshl_add_u64 v[232:233], s[54:55], 0, v[154:155]
	ds_read_b128 v[198:201], v191 offset:32768
	ds_read_b128 v[202:205], v191 offset:33792
	ds_read_b128 v[206:209], v191 offset:34816
	ds_read_b128 v[210:213], v191 offset:35840
	ds_read_b128 v[214:217], v191 offset:36864
	ds_read_b128 v[218:221], v191 offset:37888
	ds_read_b128 v[222:225], v191 offset:38912
	ds_read_b128 v[226:229], v191 offset:39936
	global_load_lds_dwordx4 v[232:233], off
	v_lshl_add_u64 v[232:233], s[54:55], 0, v[158:159]
	s_mov_b32 m0, s49
	s_nop 0
	global_load_lds_dwordx4 v[232:233], off
	s_mov_b64 vcc, s[98:99]
	s_cbranch_vccnz .Lg0skip_7
	s_waitcnt vmcnt(8)

.Lg0m_7:
	s_barrier
	s_add_i32 s2, s2, s42
	v_lshl_add_u64 v[178:179], v[178:179], 0, s[26:27]
	s_mov_b32 m0, s2
	ds_read_b128 v[198:201], v191 offset:49152
	ds_read_b128 v[202:205], v191 offset:50176
	ds_read_b128 v[206:209], v191 offset:51200
	ds_read_b128 v[210:213], v191 offset:52224
	ds_read_b128 v[214:217], v191 offset:53248
	ds_read_b128 v[218:221], v191 offset:54272
	ds_read_b128 v[222:225], v191 offset:55296
	ds_read_b128 v[226:229], v191 offset:56320
	global_load_lds_dwordx4 v[178:179], off
	s_add_i32 m0, s2, 0x2000
	s_add_u32 s54, s58, 0x80080
	v_lshl_add_u64 v[178:179], v[182:183], 0, s[26:27]
	s_addc_u32 s55, s59, 0
	s_add_i32 s2, s60, s42
	global_load_lds_dwordx4 v[178:179], off
	v_lshl_add_u64 v[178:179], s[54:55], 0, v[156:157]
	s_mov_b32 m0, s2
	s_nop 0
	global_load_lds_dwordx4 v[178:179], off
	v_lshl_add_u64 v[178:179], s[54:55], 0, v[160:161]
	s_add_i32 m0, s2, 0x2000
	s_nop 0
	global_load_lds_dwordx4 v[178:179], off
	v_lshl_add_u64 v[178:179], v[186:187], 0, s[26:27]
	s_mov_b32 m0, s51
	s_nop 0
	global_load_lds_dwordx4 v[178:179], off
	v_lshl_add_u64 v[178:179], v[230:231], 0, s[26:27]
	s_mov_b32 m0, s52
	s_nop 0
	global_load_lds_dwordx4 v[178:179], off
	s_mov_b64 vcc, s[98:99]
	s_cbranch_vccnz .Lg0skip_8
	s_waitcnt vmcnt(8)

.Lg0m_8:
	s_barrier
	s_add_i32 s68, s68, 2
	s_cmp_gt_u32 s68, 29
	s_mov_b64 s[54:55], s[56:57]
	s_cbranch_scc0 .LBB0_1547
	s_and_b64 vcc, exec, s[28:29]
	s_cbranch_vccz .LBB0_1550
	s_barrier

	.amdhsa_kernel _Z3fwd4Args
		.amdhsa_group_segment_fixed_size 0
		.amdhsa_private_segment_fixed_size 0
		.amdhsa_kernarg_size 472
		.amdhsa_user_sgpr_count 2
		.amdhsa_user_sgpr_dispatch_ptr 0
		.amdhsa_user_sgpr_queue_ptr 0
		.amdhsa_user_sgpr_kernarg_segment_ptr 1
		.amdhsa_user_sgpr_dispatch_id 0
		.amdhsa_user_sgpr_kernarg_preload_length 0
		.amdhsa_user_sgpr_kernarg_preload_offset 0
		.amdhsa_user_sgpr_private_segment_size 0
		.amdhsa_uses_dynamic_stack 0
		.amdhsa_enable_private_segment 0
		.amdhsa_system_sgpr_workgroup_id_x 1
		.amdhsa_system_sgpr_workgroup_id_y 0
		.amdhsa_system_sgpr_workgroup_id_z 0
		.amdhsa_system_sgpr_workgroup_info 0
		.amdhsa_system_vgpr_workitem_id 0
		.amdhsa_next_free_vgpr 253
		.amdhsa_next_free_sgpr 102
		.amdhsa_accum_offset 256
		.amdhsa_reserve_vcc 1
		.amdhsa_float_round_mode_32 0
		.amdhsa_float_round_mode_16_64 0
		.amdhsa_float_denorm_mode_32 3
		.amdhsa_float_denorm_mode_16_64 3
		.amdhsa_dx10_clamp 1
		.amdhsa_ieee_mode 1
		.amdhsa_fp16_overflow 0
		.amdhsa_tg_split 0
		.amdhsa_exception_fp_ieee_invalid_op 0
		.amdhsa_exception_fp_denorm_src 0
		.amdhsa_exception_fp_ieee_div_zero 0
		.amdhsa_exception_fp_ieee_overflow 0
		.amdhsa_exception_fp_ieee_underflow 0
		.amdhsa_exception_fp_ieee_inexact 0
		.amdhsa_exception_int_div_zero 0
	.end_amdhsa_kernel

amdhsa.kernels:
  - .agpr_count:     0
    .args:
      - .offset:         0
        .size:           216
        .value_kind:     by_value
      - .offset:         216
        .size:           4
        .value_kind:     hidden_block_count_x
      - .offset:         220
        .size:           4
        .value_kind:     hidden_block_count_y
      - .offset:         224
        .size:           4
        .value_kind:     hidden_block_count_z
      - .offset:         228
        .size:           2
        .value_kind:     hidden_group_size_x
      - .offset:         230
        .size:           2
        .value_kind:     hidden_group_size_y
      - .offset:         232
        .size:           2
        .value_kind:     hidden_group_size_z
      - .offset:         234
        .size:           2
        .value_kind:     hidden_remainder_x
      - .offset:         236
        .size:           2
        .value_kind:     hidden_remainder_y
      - .offset:         238
        .size:           2
        .value_kind:     hidden_remainder_z
      - .offset:         256
        .size:           8
        .value_kind:     hidden_global_offset_x
      - .offset:         264
        .size:           8
        .value_kind:     hidden_global_offset_y
      - .offset:         272
        .size:           8
        .value_kind:     hidden_global_offset_z
      - .offset:         280
        .size:           2
        .value_kind:     hidden_grid_dims
      - .offset:         336
        .size:           4
        .value_kind:     hidden_dynamic_lds_size
    .group_segment_fixed_size: 0
    .kernarg_segment_align: 8
    .kernarg_segment_size: 472
    .language:       OpenCL C
    .language_version:
      - 2
      - 0
    .max_flat_workgroup_size: 512
    .name:           _Z3fwd4Args
    .private_segment_fixed_size: 0
    .sgpr_count:     108
    .sgpr_spill_count: 68
    .symbol:         _Z3fwd4Args.kd
    .uniform_work_group_size: 1
    .uses_dynamic_stack: false
    .vgpr_count:     253
    .vgpr_spill_count: 0
    .wavefront_size: 64
